# final plus non-temporal stores for the next-layer fp8 pre-norm rows written in N2
# baseline (speedup 1.0000x reference)
; DI unsigned pk2(float lo, float hi) { f32x2 v = {lo, hi}; bf16x2v r = __builtin_convertvector(v, bf16x2v); return __builtin_bit_cast(unsigned, r); }
; DI unsigned pk4_fp8(float a, float b, float c, float d) { int r = 0; r = __builtin_amdgcn_cvt_pk_fp8_f32(sat8(a), sat8(b), r, false); r = __builtin_amdgcn_cvt_pk_fp8_f32(sat8(c), sat8(d), r, true); return (unsigned)r; }
; DI void mod_norm_store8(const f32x4 (&xv)[4], float rstd, const ModP& m, unsigned char* orow, int lane, f32x4 (&hv)[4]) {
; #pragma unroll
;     ...
;         hv[j] = xv[j] * rstd * gv * (1.0f + scv) + shv;
;         *(unsigned*)(orow + o) = pk4_fp8(hv[j][0] * H8_SCALE, hv[j][1] * H8_SCALE, hv[j][2] * H8_SCALE, hv[j][3] * H8_SCALE); }
; }
; DI void phase_n2(Frame& F, int l) {
;     ...
;             const float rstd_y = rsqrtf(sumsq(yv, F.lane) * (1.0f / D) + RMS_EPS);
; #pragma unroll
;             for (int j = 0; j < 4; ++j) { const int o = 4 * F.lane + 256 * j; const f32x4 gv = gpf[j], gt = gtf[j];
;                 xv[j] = xv[j] + gt * (yv[j] * rstd_y * gv);
;                 if (l + 1 < DEPTH) { u32x2 w; w.x = pk2(xv[j][0], xv[j][1]); w.y = pk2(xv[j][2], xv[j][3]); *(u32x2*)(xb + (size_t)r * D + o) = w; } else *(f32x4*)(F.out + (size_t)r * D + o) = xv[j]; }
;             if (l + 1 < DEPTH) { const float rstd_x = rsqrtf(sumsq(xv, F.lane) * (1.0f / D) + RMS_EPS);
;                 mod_norm_store8(xv, rstd_x, mp, F.ws + WS_HF8 + (size_t)r * D, F.lane, hv); } }
.LBB0_1418:
	v_pk_add_f32 v[134:135], v[44:45], 1.0 op_sel_hi:[1,0]
	v_pk_add_f32 v[136:137], v[42:43], 1.0 op_sel_hi:[1,0]
	v_pk_add_f32 v[130:131], v[28:29], 1.0 op_sel_hi:[1,0]
	v_pk_add_f32 v[132:133], v[26:27], 1.0 op_sel_hi:[1,0]
	v_pk_add_f32 v[126:127], v[36:37], 1.0 op_sel_hi:[1,0]
	v_pk_add_f32 v[128:129], v[34:35], 1.0 op_sel_hi:[1,0]
	v_pk_add_f32 v[122:123], v[48:49], 1.0 op_sel_hi:[1,0]
	s_and_b64 vcc, exec, s[4:5]
	v_pk_add_f32 v[124:125], v[46:47], 1.0 op_sel_hi:[1,0]
	s_cbranch_vccnz .LBB0_1420
	v_pk_mul_f32 v[154:155], v[84:85], v[84:85]
	v_pk_mul_f32 v[156:157], v[82:83], v[82:83]
	s_nop 0
	v_pk_mov_b32 v[158:159], v[156:157], v[154:155] op_sel:[1,0]
	v_mov_b32_e32 v157, v155
	v_pk_add_f32 v[154:155], v[158:159], v[156:157]
	v_pk_mul_f32 v[156:157], v[88:89], v[88:89]
	v_pk_add_f32 v[154:155], v[154:155], v[154:155] op_sel_hi:[0,1]
	v_pk_mul_f32 v[158:159], v[86:87], v[86:87]
	v_mul_f32_e32 v154, v90, v90
	v_pk_mov_b32 v[160:161], v[158:159], v[156:157] op_sel:[1,0]
	v_mov_b32_e32 v159, v157
	v_pk_add_f32 v[156:157], v[160:161], v[158:159]
	v_pk_fma_f32 v[158:159], v[90:91], v[90:91], v[154:155] op_sel_hi:[1,1,0]
	v_mul_f32_e32 v154, v92, v92
	v_pk_add_f32 v[156:157], v[156:157], v[156:157] op_sel_hi:[0,1]
	v_pk_fma_f32 v[160:161], v[92:93], v[92:93], v[154:155] op_sel_hi:[1,1,0]
	v_mul_f32_e32 v158, v94, v94
	v_mul_f32_e32 v160, v95, v95
	v_mul_f32_e32 v154, v96, v96
	v_mul_f32_e32 v156, v97, v97
	v_pk_add_f32 v[158:159], v[158:159], v[160:161]
	v_pk_add_f32 v[154:155], v[154:155], v[156:157]
	s_nop 0
	v_pk_add_f32 v[154:155], v[158:159], v[154:155]
	s_nop 0
	v_add_f32_e32 v153, v154, v155
	v_mov_b32_e32 v154, v1
	s_nop 0
	v_add_f32_dpp v153, v153, v153 row_shr:1 row_mask:0xf bank_mask:0xf bound_ctrl:1
	s_nop 1
	v_add_f32_dpp v153, v153, v153 row_shr:2 row_mask:0xf bank_mask:0xf bound_ctrl:1
	s_nop 1
	v_add_f32_dpp v153, v153, v153 row_shr:4 row_mask:0xf bank_mask:0xf bound_ctrl:1
	s_nop 1
	v_add_f32_dpp v153, v153, v153 row_shr:8 row_mask:0xf bank_mask:0xf bound_ctrl:1
	s_nop 1
	v_mov_b32_dpp v154, v153 row_bcast:15 row_mask:0xa bank_mask:0xf
	v_add_f32_e32 v153, v153, v154
	v_mov_b32_e32 v154, v1
	s_nop 1
	v_mov_b32_dpp v154, v153 row_bcast:31 row_mask:0xc bank_mask:0xf
	v_add_f32_e32 v153, v153, v154
	v_mov_b32_e32 v154, 0x3a800000
	v_readlane_b32 s0, v153, 63
	v_mov_b32_e32 v153, 0x358637bd
	s_nop 0
	v_fma_f32 v153, s0, v154, v153
	v_mul_f32_e32 v154, 0x4b800000, v153
	v_cmp_gt_f32_e32 vcc, s51, v153
	v_readlane_b32 s0, v253, 8
	v_readlane_b32 s2, v253, 10
	v_cndmask_b32_e32 v153, v153, v154, vcc
	v_rsq_f32_e32 v153, v153
	v_readlane_b32 s3, v253, 11
	v_readlane_b32 s1, v253, 9
	v_mul_f32_e32 v154, 0x45800000, v153
	v_cndmask_b32_e32 v154, v153, v154, vcc
	v_pk_mul_f32 v[82:83], v[82:83], v[154:155] op_sel_hi:[1,0]
	v_pk_mul_f32 v[84:85], v[84:85], v[154:155] op_sel_hi:[1,0]
	v_pk_mul_f32 v[82:83], v[18:19], v[82:83]
	v_pk_mul_f32 v[86:87], v[86:87], v[154:155] op_sel_hi:[1,0]
	v_pk_mul_f32 v[84:85], v[20:21], v[84:85]
	v_pk_fma_f32 v[82:83], v[136:137], v[82:83], v[30:31]
	v_pk_mul_f32 v[86:87], v[2:3], v[86:87]
	v_pk_fma_f32 v[84:85], v[134:135], v[84:85], v[32:33]
	v_mul_f32_e32 v82, 0x41800000, v82
	v_mul_f32_e32 v83, 0x41800000, v83
	v_pk_fma_f32 v[86:87], v[132:133], v[86:87], v[10:11]
	v_mul_f32_e32 v84, 0x41800000, v84
	v_med3_f32 v82, v82, s53, v204
	v_med3_f32 v83, v83, s53, v204
	v_mov_b32_e32 v153, v1
	v_mul_f32_e32 v86, 0x41800000, v86
	v_mul_f32_e32 v87, 0x41800000, v87
	v_cvt_pk_fp8_f32 v153, v82, v83
	v_mul_f32_e32 v82, 0x41800000, v85
	v_med3_f32 v83, v84, s53, v204
	v_pk_mul_f32 v[84:85], v[88:89], v[154:155] op_sel_hi:[1,0]
	v_med3_f32 v86, v86, s53, v204
	v_med3_f32 v87, v87, s53, v204
	v_mov_b32_e32 v88, v1
	v_pk_mul_f32 v[84:85], v[4:5], v[84:85]
	v_cvt_pk_fp8_f32 v88, v86, v87
	v_pk_mul_f32 v[86:87], v[90:91], v[154:155] op_sel_hi:[1,0]
	v_pk_fma_f32 v[84:85], v[130:131], v[84:85], v[12:13]
	v_pk_mul_f32 v[86:87], v[14:15], v[86:87]
	v_mul_f32_e32 v84, 0x41800000, v84
	v_mul_f32_e32 v85, 0x41800000, v85
	v_pk_fma_f32 v[86:87], v[128:129], v[86:87], v[6:7]
	v_med3_f32 v84, v84, s53, v204
	v_med3_f32 v85, v85, s53, v204
	v_mul_f32_e32 v86, 0x41800000, v86
	v_mul_f32_e32 v87, 0x41800000, v87
	v_cvt_pk_fp8_f32 v88, v84, v85 op_sel:[0,0,1]
	v_pk_mul_f32 v[84:85], v[92:93], v[154:155] op_sel_hi:[1,0]
	v_med3_f32 v86, v86, s53, v204
	v_med3_f32 v87, v87, s53, v204
	v_mov_b32_e32 v89, v1
	v_pk_mul_f32 v[84:85], v[16:17], v[84:85]
	v_cvt_pk_fp8_f32 v89, v86, v87
	v_pk_mul_f32 v[86:87], v[94:95], v[154:155] op_sel_hi:[1,0]
	v_pk_fma_f32 v[84:85], v[126:127], v[84:85], v[8:9]
	v_pk_mul_f32 v[86:87], v[38:39], v[86:87]
	v_mul_f32_e32 v84, 0x41800000, v84
	v_mul_f32_e32 v85, 0x41800000, v85
	v_pk_fma_f32 v[86:87], v[124:125], v[86:87], v[22:23]
	v_med3_f32 v84, v84, s53, v204
	v_med3_f32 v85, v85, s53, v204
	v_mul_f32_e32 v86, 0x41800000, v86
	v_mul_f32_e32 v87, 0x41800000, v87
	v_cvt_pk_fp8_f32 v89, v84, v85 op_sel:[0,0,1]
	v_pk_mul_f32 v[84:85], v[96:97], v[154:155] op_sel_hi:[1,0]
	v_med3_f32 v86, v86, s53, v204
	v_med3_f32 v87, v87, s53, v204
	v_mov_b32_e32 v90, v1
	v_med3_f32 v82, v82, s53, v204
	v_pk_mul_f32 v[84:85], v[40:41], v[84:85]
	v_cvt_pk_fp8_f32 v90, v86, v87
	v_cvt_pk_fp8_f32 v153, v83, v82 op_sel:[0,0,1]
	v_pk_fma_f32 v[84:85], v[122:123], v[84:85], v[24:25]
	v_lshl_add_u64 v[82:83], s[2:3], 0, v[104:105]
	v_mul_f32_e32 v84, 0x41800000, v84
	v_mul_f32_e32 v85, 0x41800000, v85
	v_add_co_u32_e32 v82, vcc, s33, v82
	v_med3_f32 v84, v84, s53, v204
	v_med3_f32 v85, v85, s53, v204
	v_addc_co_u32_e32 v83, vcc, 0, v83, vcc
	v_cvt_pk_fp8_f32 v90, v84, v85 op_sel:[0,0,1]
	global_store_dword v[82:83], v153, off nt
	global_store_dword v[82:83], v88, off offset:256 nt
	global_store_dword v[82:83], v89, off offset:512 nt
	global_store_dword v[82:83], v90, off offset:768 nt

; DI unsigned pk4_fp8(float a, float b, float c, float d) { int r = 0; r = __builtin_amdgcn_cvt_pk_fp8_f32(sat8(a), sat8(b), r, false); r = __builtin_amdgcn_cvt_pk_fp8_f32(sat8(c), sat8(d), r, true); return (unsigned)r; }
; DI void mod_norm_store8(const f32x4 (&xv)[4], float rstd, const ModP& m, unsigned char* orow, int lane, f32x4 (&hv)[4]) {
; #pragma unroll
;     ...
;         hv[j] = xv[j] * rstd * gv * (1.0f + scv) + shv;
;         *(unsigned*)(orow + o) = pk4_fp8(hv[j][0] * H8_SCALE, hv[j][1] * H8_SCALE, hv[j][2] * H8_SCALE, hv[j][3] * H8_SCALE); }
; }
; DI void phase_n2(Frame& F, int l) {
;     ...
;             if (l + 1 < DEPTH) { const float rstd_x = rsqrtf(sumsq(xv, F.lane) * (1.0f / D) + RMS_EPS);
;                 mod_norm_store8(xv, rstd_x, mp, F.ws + WS_HF8 + (size_t)r * D, F.lane, hv); } }
.LBB0_1437:
	v_pk_mul_f32 v[54:55], v[76:77], v[76:77]
	v_pk_mul_f32 v[56:57], v[74:75], v[74:75]
	v_mul_f32_e32 v0, v58, v58
	v_pk_mov_b32 v[62:63], v[56:57], v[54:55] op_sel:[1,0]
	v_mov_b32_e32 v57, v55
	v_pk_add_f32 v[54:55], v[62:63], v[56:57]
	v_pk_mul_f32 v[56:57], v[68:69], v[68:69]
	v_pk_mul_f32 v[62:63], v[66:67], v[66:67]
	v_pk_add_f32 v[54:55], v[54:55], v[54:55] op_sel_hi:[0,1]
	v_pk_mov_b32 v[64:65], v[62:63], v[56:57] op_sel:[1,0]
	v_mov_b32_e32 v63, v57
	v_pk_add_f32 v[56:57], v[64:65], v[62:63]
	v_pk_fma_f32 v[62:63], v[58:59], v[58:59], v[0:1] op_sel_hi:[1,1,0]
	v_mul_f32_e32 v0, v60, v60
	v_pk_add_f32 v[56:57], v[56:57], v[56:57] op_sel_hi:[0,1]
	v_pk_fma_f32 v[64:65], v[60:61], v[60:61], v[0:1] op_sel_hi:[1,1,0]
	v_mul_f32_e32 v62, v50, v50
	v_mul_f32_e32 v64, v51, v51
	v_mul_f32_e32 v54, v52, v52
	v_mul_f32_e32 v56, v53, v53
	v_pk_add_f32 v[62:63], v[62:63], v[64:65]
	v_pk_add_f32 v[54:55], v[54:55], v[56:57]
	v_mov_b32_e32 v64, v1
	v_pk_add_f32 v[54:55], v[62:63], v[54:55]
	v_mov_b32_e32 v65, v1
	v_add_f32_e32 v0, v54, v55
	v_mov_b32_e32 v54, v1
	s_nop 0
	v_add_f32_dpp v0, v0, v0 row_shr:1 row_mask:0xf bank_mask:0xf bound_ctrl:1
	s_nop 1
	v_add_f32_dpp v0, v0, v0 row_shr:2 row_mask:0xf bank_mask:0xf bound_ctrl:1
	s_nop 1
	v_add_f32_dpp v0, v0, v0 row_shr:4 row_mask:0xf bank_mask:0xf bound_ctrl:1
	s_nop 1
	v_add_f32_dpp v0, v0, v0 row_shr:8 row_mask:0xf bank_mask:0xf bound_ctrl:1
	s_nop 1
	v_mov_b32_dpp v54, v0 row_bcast:15 row_mask:0xa bank_mask:0xf
	v_add_f32_e32 v0, v0, v54
	v_mov_b32_e32 v54, v1
	s_nop 1
	v_mov_b32_dpp v54, v0 row_bcast:31 row_mask:0xc bank_mask:0xf
	v_add_f32_e32 v0, v0, v54
	v_mov_b32_e32 v54, 0x3a800000
	v_readlane_b32 s0, v0, 63
	v_mov_b32_e32 v0, 0x358637bd
	s_nop 0
	v_fma_f32 v0, s0, v54, v0
	v_mul_f32_e32 v54, 0x4b800000, v0
	v_cmp_gt_f32_e32 vcc, s51, v0
	v_readlane_b32 s0, v253, 8
	v_readlane_b32 s2, v253, 10
	v_cndmask_b32_e32 v0, v0, v54, vcc
	v_rsq_f32_e32 v0, v0
	v_readlane_b32 s3, v253, 11
	v_readlane_b32 s1, v253, 9
	v_mul_f32_e32 v54, 0x45800000, v0
	v_cndmask_b32_e32 v0, v0, v54, vcc
	v_pk_mul_f32 v[56:57], v[74:75], v[0:1] op_sel_hi:[1,0]
	v_pk_mul_f32 v[62:63], v[66:67], v[0:1] op_sel_hi:[1,0]
	v_pk_mul_f32 v[56:57], v[18:19], v[56:57]
	v_pk_mul_f32 v[62:63], v[2:3], v[62:63]
	v_pk_fma_f32 v[56:57], v[136:137], v[56:57], v[30:31]
	v_pk_fma_f32 v[62:63], v[132:133], v[62:63], v[10:11]
	v_mul_f32_e32 v56, 0x41800000, v56
	v_mul_f32_e32 v57, 0x41800000, v57
	v_med3_f32 v56, v56, s53, v204
	v_med3_f32 v57, v57, s53, v204
	v_mul_f32_e32 v62, 0x41800000, v62
	v_mul_f32_e32 v63, 0x41800000, v63
	v_cvt_pk_fp8_f32 v64, v56, v57
	v_pk_mul_f32 v[56:57], v[68:69], v[0:1] op_sel_hi:[1,0]
	v_med3_f32 v62, v62, s53, v204
	v_med3_f32 v63, v63, s53, v204
	v_pk_mul_f32 v[56:57], v[4:5], v[56:57]
	v_cvt_pk_fp8_f32 v65, v62, v63
	v_pk_mul_f32 v[58:59], v[58:59], v[0:1] op_sel_hi:[1,0]
	v_pk_fma_f32 v[56:57], v[130:131], v[56:57], v[12:13]
	v_pk_mul_f32 v[58:59], v[14:15], v[58:59]
	v_pk_mul_f32 v[50:51], v[50:51], v[0:1] op_sel_hi:[1,0]
	v_pk_mul_f32 v[54:55], v[76:77], v[0:1] op_sel_hi:[1,0]
	v_mul_f32_e32 v56, 0x41800000, v56
	v_mul_f32_e32 v57, 0x41800000, v57
	v_pk_fma_f32 v[58:59], v[128:129], v[58:59], v[6:7]
	v_pk_mul_f32 v[52:53], v[52:53], v[0:1] op_sel_hi:[1,0]
	v_pk_mul_f32 v[50:51], v[38:39], v[50:51]
	v_pk_mul_f32 v[54:55], v[20:21], v[54:55]
	v_med3_f32 v56, v56, s53, v204
	v_med3_f32 v57, v57, s53, v204
	v_mul_f32_e32 v58, 0x41800000, v58
	v_mul_f32_e32 v59, 0x41800000, v59
	v_pk_mul_f32 v[52:53], v[40:41], v[52:53]
	v_pk_fma_f32 v[50:51], v[124:125], v[50:51], v[22:23]
	v_pk_fma_f32 v[54:55], v[134:135], v[54:55], v[32:33]
	v_cvt_pk_fp8_f32 v65, v56, v57 op_sel:[0,0,1]
	v_pk_mul_f32 v[56:57], v[60:61], v[0:1] op_sel_hi:[1,0]
	v_med3_f32 v58, v58, s53, v204
	v_med3_f32 v59, v59, s53, v204
	v_mov_b32_e32 v60, v1
	v_pk_fma_f32 v[52:53], v[122:123], v[52:53], v[24:25]
	v_mul_f32_e32 v0, 0x41800000, v50
	v_mul_f32_e32 v50, 0x41800000, v51
	v_mul_f32_e32 v54, 0x41800000, v54
	v_mul_f32_e32 v55, 0x41800000, v55
	v_pk_mul_f32 v[56:57], v[16:17], v[56:57]
	v_cvt_pk_fp8_f32 v60, v58, v59
	v_mul_f32_e32 v51, 0x41800000, v52
	v_med3_f32 v0, v0, s53, v204
	v_med3_f32 v50, v50, s53, v204
	v_mov_b32_e32 v52, v1
	v_med3_f32 v54, v54, s53, v204
	v_med3_f32 v55, v55, s53, v204
	v_pk_fma_f32 v[56:57], v[126:127], v[56:57], v[8:9]
	v_cvt_pk_fp8_f32 v52, v0, v50
	v_cvt_pk_fp8_f32 v64, v54, v55 op_sel:[0,0,1]
	v_mul_f32_e32 v56, 0x41800000, v56
	v_mul_f32_e32 v57, 0x41800000, v57
	v_lshl_add_u64 v[54:55], s[2:3], 0, v[104:105]
	v_med3_f32 v56, v56, s53, v204
	v_med3_f32 v57, v57, s53, v204
	v_mul_f32_e32 v0, 0x41800000, v53
	v_add_co_u32_e32 v54, vcc, s33, v54
	v_cvt_pk_fp8_f32 v60, v56, v57 op_sel:[0,0,1]
	v_med3_f32 v50, v51, s53, v204
	v_med3_f32 v0, v0, s53, v204
	v_addc_co_u32_e32 v55, vcc, 0, v55, vcc
	v_cvt_pk_fp8_f32 v52, v50, v0 op_sel:[0,0,1]
	global_store_dword v[54:55], v64, off offset:1024 nt
	global_store_dword v[54:55], v65, off offset:1280 nt
	global_store_dword v[54:55], v60, off offset:1536 nt
	global_store_dword v[54:55], v52, off offset:1792 nt
	s_branch .LBB0_1399
